# baseline (speedup 1.0000x reference)
.LBB4_6:
	s_waitcnt lgkmcnt(1)
	s_nop 0
	v_mfma_f32_16x16x32_f16 v[66:69], v[10:13], v[26:29], v[66:69]
	v_bfe_u32 v84, v0, 4, 2
	s_load_dwordx4 s[4:7], s[0:1], 0x18
	s_add_i32 s0, s24, s10
	v_mfma_f32_16x16x32_f16 v[58:61], v[14:17], v[26:29], v[58:61]
	v_lshlrev_b32_e32 v84, 2, v84
	s_movk_i32 s9, 0xffd0
	s_waitcnt lgkmcnt(0)
	v_mfma_f32_16x16x32_f16 v[26:29], v[6:9], v[26:29], v[50:53]
	v_mfma_f32_16x16x32_f16 v[34:37], v[10:13], v[22:25], v[34:37]
	v_mfma_f32_16x16x32_f16 v[42:45], v[14:17], v[22:25], v[42:45]
	v_mfma_f32_16x16x32_f16 v[22:25], v[6:9], v[22:25], v[46:49]
	s_nop 2
	ds_read_b128 v[46:49], v83 offset:16384
	ds_read_b128 v[50:53], v83 offset:18432
	v_mfma_f32_16x16x32_f16 v[30:33], v[10:13], v[18:21], v[30:33]
	v_mfma_f32_16x16x32_f16 v[38:41], v[14:17], v[18:21], v[38:41]
	v_mfma_f32_16x16x32_f16 v[18:21], v[6:9], v[18:21], v[54:57]
	v_mfma_f32_16x16x32_f16 v[10:13], v[10:13], v[2:5], v[70:73]
	v_mfma_f32_16x16x32_f16 v[14:17], v[14:17], v[2:5], v[74:77]
	s_nop 1
	v_add_u32_e32 v70, 0x14000, v78
	v_mfma_f32_16x16x32_f16 v[2:5], v[6:9], v[2:5], v[62:65]
	ds_read_b128 v[6:9], v78
	ds_read_b128 v[54:57], v78 offset:2048
	v_add_u32_e32 v74, 0x15000, v79
	v_add_u32_e32 v75, 0x15800, v79
	s_waitcnt lgkmcnt(1)
	v_mfma_f32_16x16x32_f16 v[62:65], v[46:49], v[6:9], v[66:69]
	s_nop 2
	ds_read_b128 v[66:69], v83 offset:20480
	v_mfma_f32_16x16x32_f16 v[58:61], v[50:53], v[6:9], v[58:61]
	s_waitcnt lgkmcnt(0)
	v_mfma_f32_16x16x32_f16 v[6:9], v[66:69], v[6:9], v[26:29]
	v_mfma_f32_16x16x32_f16 v[26:29], v[46:49], v[54:57], v[34:37]
	v_mfma_f32_16x16x32_f16 v[34:37], v[50:53], v[54:57], v[42:45]
	v_mfma_f32_16x16x32_f16 v[22:25], v[66:69], v[54:57], v[22:25]
	s_nop 1
	ds_read_b128 v[42:45], v78 offset:4096
	ds_read_b128 v[54:57], v78 offset:6144
	s_waitcnt vmcnt(5) lgkmcnt(0)
	s_barrier
	s_waitcnt lgkmcnt(1)
	v_mfma_f32_16x16x32_f16 v[30:33], v[46:49], v[42:45], v[30:33]
	v_mfma_f32_16x16x32_f16 v[38:41], v[50:53], v[42:45], v[38:41]
	v_mfma_f32_16x16x32_f16 v[18:21], v[66:69], v[42:45], v[18:21]
	s_waitcnt lgkmcnt(0)
	v_mfma_f32_16x16x32_f16 v[10:13], v[46:49], v[54:57], v[10:13]
	ds_read_b128 v[42:45], v81 offset:57344
	ds_read_b128 v[46:49], v81 offset:59392
	v_mfma_f32_16x16x32_f16 v[14:17], v[50:53], v[54:57], v[14:17]
	v_mfma_f32_16x16x32_f16 v[2:5], v[66:69], v[54:57], v[2:5]
	ds_read_b128 v[50:53], v79 offset:40960
	ds_read_b128 v[54:57], v81 offset:61440
	s_waitcnt lgkmcnt(1)
	v_mfma_f32_16x16x32_f16 v[62:65], v[42:45], v[50:53], v[62:65]
	v_mfma_f32_16x16x32_f16 v[58:61], v[46:49], v[50:53], v[58:61]
	s_waitcnt lgkmcnt(0)
	v_mfma_f32_16x16x32_f16 v[6:9], v[54:57], v[50:53], v[6:9]
	ds_read_b128 v[50:53], v79 offset:43008
	ds_read_b128 v[66:69], v79 offset:45056
	s_waitcnt lgkmcnt(1)
	v_mfma_f32_16x16x32_f16 v[26:29], v[42:45], v[50:53], v[26:29]
	v_mfma_f32_16x16x32_f16 v[34:37], v[46:49], v[50:53], v[34:37]
	v_mfma_f32_16x16x32_f16 v[22:25], v[54:57], v[50:53], v[22:25]
	s_waitcnt lgkmcnt(0)
	v_mfma_f32_16x16x32_f16 v[30:33], v[42:45], v[66:69], v[30:33]
	v_mfma_f32_16x16x32_f16 v[38:41], v[46:49], v[66:69], v[38:41]
	v_mfma_f32_16x16x32_f16 v[18:21], v[54:57], v[66:69], v[18:21]
	ds_read_b128 v[50:53], v79 offset:47104
	ds_read_b128 v[66:69], v78 offset:40960
	s_waitcnt lgkmcnt(1)
	v_mfma_f32_16x16x32_f16 v[10:13], v[42:45], v[50:53], v[10:13]
	ds_read_b128 v[42:45], v83 offset:57344
	v_mfma_f32_16x16x32_f16 v[14:17], v[46:49], v[50:53], v[14:17]
	ds_read_b128 v[46:49], v83 offset:59392
	v_mfma_f32_16x16x32_f16 v[2:5], v[54:57], v[50:53], v[2:5]
	ds_read_b128 v[54:57], v83 offset:61440
	v_add_u32_e32 v83, 0x14000, v82
	s_waitcnt lgkmcnt(2)
	v_mfma_f32_16x16x32_f16 v[50:53], v[42:45], v[66:69], v[62:65]
	s_waitcnt lgkmcnt(1)
	v_mfma_f32_16x16x32_f16 v[58:61], v[46:49], v[66:69], v[58:61]
	s_waitcnt lgkmcnt(0)
	v_mfma_f32_16x16x32_f16 v[6:9], v[54:57], v[66:69], v[6:9]
	ds_read_b128 v[62:65], v78 offset:43008
	ds_read_b128 v[66:69], v78 offset:45056
	s_waitcnt lgkmcnt(1)
	v_mfma_f32_16x16x32_f16 v[26:29], v[42:45], v[62:65], v[26:29]
	v_mfma_f32_16x16x32_f16 v[34:37], v[46:49], v[62:65], v[34:37]
	v_mfma_f32_16x16x32_f16 v[22:25], v[54:57], v[62:65], v[22:25]
	ds_read_b128 v[62:65], v78 offset:47104
	s_waitcnt vmcnt(0) lgkmcnt(0)
	s_barrier
	s_waitcnt lgkmcnt(1)
	v_mfma_f32_16x16x32_f16 v[30:33], v[42:45], v[66:69], v[30:33]
	v_mfma_f32_16x16x32_f16 v[38:41], v[46:49], v[66:69], v[38:41]
	v_mfma_f32_16x16x32_f16 v[18:21], v[54:57], v[66:69], v[18:21]
	v_add_u32_e32 v66, 0x14000, v79
	v_add_u32_e32 v67, 0x14800, v80
	s_waitcnt lgkmcnt(0)
	v_mfma_f32_16x16x32_f16 v[10:13], v[42:45], v[62:65], v[10:13]
	v_add_u32_e32 v42, 0x14000, v80
	ds_read_b128 v[42:45], v42
	v_mfma_f32_16x16x32_f16 v[14:17], v[46:49], v[62:65], v[14:17]
	ds_read_b128 v[46:49], v66
	v_add_u32_e32 v66, 0x14800, v79
	v_add_u32_e32 v79, 0x14800, v78
	v_mfma_f32_16x16x32_f16 v[2:5], v[54:57], v[62:65], v[2:5]
	ds_read_b128 v[54:57], v67
	ds_read_b128 v[62:65], v66
	v_add_u32_e32 v66, 0x15000, v80
	ds_read_b128 v[66:69], v66
	ds_read_b128 v[70:73], v70
	v_add_u32_e32 v80, 0x15000, v78
	v_add_u32_e32 v78, 0x15800, v78
	s_waitcnt lgkmcnt(4)
	v_mfma_f32_16x16x32_f16 v[50:53], v[42:45], v[46:49], v[50:53]
	s_waitcnt lgkmcnt(3)
	v_mfma_f32_16x16x32_f16 v[58:61], v[54:57], v[46:49], v[58:61]
	s_waitcnt lgkmcnt(1)
	v_mfma_f32_16x16x32_f16 v[6:9], v[66:69], v[46:49], v[6:9]
	ds_read_b128 v[46:49], v74
	ds_read_b128 v[74:77], v75
	ds_read_b128 v[86:89], v79
	ds_read_b128 v[90:93], v80
	ds_read_b128 v[78:81], v78
	ds_read_b128 v[94:97], v83
	v_add_u32_e32 v83, 0x14800, v82
	v_add_u32_e32 v82, 0x15000, v82
	v_mfma_f32_16x16x32_f16 v[26:29], v[42:45], v[62:65], v[26:29]
	v_mfma_f32_16x16x32_f16 v[34:37], v[54:57], v[62:65], v[34:37]
	v_mfma_f32_16x16x32_f16 v[22:25], v[66:69], v[62:65], v[22:25]
	ds_read_b128 v[62:65], v83
	ds_read_b128 v[98:101], v82
	v_or_b32_e32 v82, s0, v84
	v_ashrrev_i32_e32 v83, 31, v82
	s_barrier
	v_lshl_add_u64 v[82:83], v[82:83], 2, s[14:15]
	s_waitcnt lgkmcnt(7)
	v_mfma_f32_16x16x32_f16 v[30:33], v[42:45], v[46:49], v[30:33]
	s_movk_i32 s0, 0x310
	v_mul_lo_u32 v1, v1, s0
	s_lshl_b64 s[0:1], s[10:11], 2
	v_mfma_f32_16x16x32_f16 v[38:41], v[54:57], v[46:49], v[38:41]
	s_add_u32 s12, s12, s0
	s_addc_u32 s13, s13, s1
	v_mfma_f32_16x16x32_f16 v[18:21], v[66:69], v[46:49], v[18:21]
	global_load_dwordx4 v[46:49], v[82:83], off
	s_waitcnt lgkmcnt(6)
	v_mfma_f32_16x16x32_f16 v[10:13], v[42:45], v[74:77], v[10:13]
	global_load_dwordx4 v[42:45], v[82:83], off offset:64
	v_mfma_f32_16x16x32_f16 v[14:17], v[54:57], v[74:77], v[14:17]
	global_load_dwordx4 v[54:57], v[82:83], off offset:128
	v_or_b32_e32 v82, s24, v84
	v_lshlrev_b32_e32 v82, 2, v82
	s_waitcnt lgkmcnt(2)
	v_mfma_f32_16x16x32_f16 v[10:13], v[94:97], v[78:81], v[10:13]
	v_add3_u32 v1, 0, v82, v1
	s_waitcnt lgkmcnt(0)
	v_mfma_f32_16x16x32_f16 v[6:9], v[98:101], v[70:73], v[6:9]
	v_mfma_f32_16x16x32_f16 v[26:29], v[94:97], v[86:89], v[26:29]
	s_waitcnt vmcnt(2)
	s_nop 2
	v_pk_add_f32 v[12:13], v[48:49], v[12:13]
	v_pk_add_f32 v[10:11], v[46:47], v[10:11]
	ds_write_b128 v1, v[10:13] offset:37632
	v_mfma_f32_16x16x32_f16 v[10:13], v[62:65], v[70:73], v[58:61]
	v_add_f32_e64 v28, v48, v28
	v_add_f32_e64 v29, v49, v29
	v_pk_add_f32 v[26:27], v[46:47], v[26:27]
	ds_write_b128 v1, v[26:29] offset:12544
	v_mfma_f32_16x16x32_f16 v[2:5], v[66:69], v[74:77], v[2:5]
	s_waitcnt vmcnt(0)
	v_pk_add_f32 v[8:9], v[56:57], v[8:9]
	s_nop 0
	v_pk_add_f32 v[12:13], v[44:45], v[12:13]
	v_pk_add_f32 v[10:11], v[42:43], v[10:11]
	ds_write_b128 v1, v[10:13] offset:64
	v_mfma_f32_16x16x32_f16 v[10:13], v[62:65], v[86:89], v[34:37]
	v_add_f32_e64 v6, v54, v6
	v_add_f32_e64 v7, v55, v7
	ds_write_b128 v1, v[6:9] offset:128
	v_mfma_f32_16x16x32_f16 v[6:9], v[98:101], v[86:89], v[22:25]
	v_mfma_f32_16x16x32_f16 v[50:53], v[94:97], v[70:73], v[50:53]
	s_nop 2
	v_add_f32_e64 v12, v44, v12
	v_add_f32_e64 v13, v45, v13
	v_pk_add_f32 v[10:11], v[42:43], v[10:11]
	ds_write_b128 v1, v[10:13] offset:12608
	v_mfma_f32_16x16x32_f16 v[10:13], v[62:65], v[90:93], v[38:41]
	v_add_f32_e64 v8, v56, v8
	v_add_f32_e64 v9, v57, v9
	v_pk_add_f32 v[6:7], v[54:55], v[6:7]
	ds_write_b128 v1, v[6:9] offset:12672
	v_mfma_f32_16x16x32_f16 v[26:29], v[94:97], v[90:93], v[30:33]
	v_add_f32_e64 v52, v48, v52
	v_add_f32_e64 v53, v49, v53
	s_nop 0
	v_pk_add_f32 v[12:13], v[44:45], v[12:13]
	v_pk_add_f32 v[10:11], v[42:43], v[10:11]
	ds_write_b128 v1, v[10:13] offset:25152
	v_mfma_f32_16x16x32_f16 v[10:13], v[62:65], v[78:81], v[14:17]
	v_add_f32_e64 v50, v46, v50
	v_add_f32_e64 v51, v47, v51
	v_pk_add_f32 v[28:29], v[48:49], v[28:29]
	v_pk_add_f32 v[26:27], v[46:47], v[26:27]
	v_mfma_f32_16x16x32_f16 v[6:9], v[98:101], v[90:93], v[18:21]
	ds_write_b128 v1, v[50:53]
	s_nop 1
	v_pk_add_f32 v[12:13], v[44:45], v[12:13]
	v_pk_add_f32 v[10:11], v[42:43], v[10:11]
	v_mfma_f32_16x16x32_f16 v[2:5], v[98:101], v[78:81], v[2:5]
	ds_write_b128 v1, v[26:29] offset:25088
	s_nop 0
	v_pk_add_f32 v[8:9], v[56:57], v[8:9]
	v_pk_add_f32 v[6:7], v[54:55], v[6:7]
	ds_write_b128 v1, v[10:13] offset:37696
	ds_write_b128 v1, v[6:9] offset:25216
	s_nop 1
	v_pk_add_f32 v[4:5], v[56:57], v[4:5]
	v_pk_add_f32 v[2:3], v[54:55], v[2:3]
	ds_write_b128 v1, v[2:5] offset:37760
	v_mul_u32_u24_e32 v1, 0xaaab, v0
	v_lshrrev_b32_e32 v1, 21, v1
	v_mul_i32_i24_e32 v2, 0xffffffd0, v1
	v_or_b32_e32 v3, s3, v1
	v_mad_i64_i32 v[30:31], s[0:1], v3, s8, 0
	v_add_lshl_u32 v2, v2, v0, 2
	v_ashrrev_i32_e32 v3, 31, v2
	v_lshl_add_u64 v[4:5], v[30:31], 2, s[12:13]
	s_waitcnt lgkmcnt(0)
	s_barrier
	s_mul_i32 s70, s3, s8
	s_lshl_b32 s71, s70, 2
	s_add_u32 s72, s12, s71
	s_addc_u32 s73, s13, 0
	s_add_u32 s70, s70, s10
	s_lshl_b32 s71, s70, 1
	s_add_u32 s74, s4, s71
	s_addc_u32 s75, s5, 0
	v_mov_b32_e32 v74, v0
	v_mul_u32_u24_e32 v75, 0xaab, v74
	v_lshrrev_b32_e32 v75, 17, v75
	v_mad_i32_i24 v76, v75, s9, v74
	v_mul_u32_u24_e32 v50, 0x300, v75
	v_lshl_add_u32 v50, v76, 2, v50
	v_mul_u32_u24_e32 v62, 0x310, v75
	v_lshl_add_u32 v62, v76, 4, v62
	v_lshlrev_b32_e32 v74, 2, v50
	global_load_dwordx4 v[2:5], v74, s[72:73] nt
	ds_read_b128 v[80:83], v62
	v_lshlrev_b32_e32 v50, 1, v50
	v_or_b32_e32 v74, 512, v0
	v_mul_u32_u24_e32 v75, 0xaab, v74
	v_lshrrev_b32_e32 v75, 17, v75
	v_mad_i32_i24 v76, v75, s9, v74
	v_mul_u32_u24_e32 v51, 0x300, v75
	v_lshl_add_u32 v51, v76, 2, v51
	v_mul_u32_u24_e32 v63, 0x310, v75
	v_lshl_add_u32 v63, v76, 4, v63
	v_lshlrev_b32_e32 v74, 2, v51
	global_load_dwordx4 v[6:9], v74, s[72:73] nt
	ds_read_b128 v[84:87], v63
	v_lshlrev_b32_e32 v51, 1, v51
	v_or_b32_e32 v74, 1024, v0
	v_mul_u32_u24_e32 v75, 0xaab, v74
	v_lshrrev_b32_e32 v75, 17, v75
	v_mad_i32_i24 v76, v75, s9, v74
	v_mul_u32_u24_e32 v52, 0x300, v75
	v_lshl_add_u32 v52, v76, 2, v52
	v_mul_u32_u24_e32 v64, 0x310, v75
	v_lshl_add_u32 v64, v76, 4, v64
	v_lshlrev_b32_e32 v74, 2, v52
	global_load_dwordx4 v[10:13], v74, s[72:73] nt
	ds_read_b128 v[88:91], v64
	v_lshlrev_b32_e32 v52, 1, v52
	v_or_b32_e32 v74, 1536, v0
	v_mul_u32_u24_e32 v75, 0xaab, v74
	v_lshrrev_b32_e32 v75, 17, v75
	v_mad_i32_i24 v76, v75, s9, v74
	v_mul_u32_u24_e32 v53, 0x300, v75
	v_lshl_add_u32 v53, v76, 2, v53
	v_mul_u32_u24_e32 v65, 0x310, v75
	v_lshl_add_u32 v65, v76, 4, v65
	v_lshlrev_b32_e32 v74, 2, v53
	global_load_dwordx4 v[14:17], v74, s[72:73] nt
	ds_read_b128 v[92:95], v65
	v_lshlrev_b32_e32 v53, 1, v53
	v_or_b32_e32 v74, 2048, v0
	v_mul_u32_u24_e32 v75, 0xaab, v74
	v_lshrrev_b32_e32 v75, 17, v75
	v_mad_i32_i24 v76, v75, s9, v74
	v_mul_u32_u24_e32 v54, 0x300, v75
	v_lshl_add_u32 v54, v76, 2, v54
	v_mul_u32_u24_e32 v66, 0x310, v75
	v_lshl_add_u32 v66, v76, 4, v66
	v_lshlrev_b32_e32 v74, 2, v54
	global_load_dwordx4 v[18:21], v74, s[72:73] nt
	ds_read_b128 v[96:99], v66
	v_lshlrev_b32_e32 v54, 1, v54
	v_or_b32_e32 v74, 2560, v0
	v_mul_u32_u24_e32 v75, 0xaab, v74
	v_lshrrev_b32_e32 v75, 17, v75
	v_mad_i32_i24 v76, v75, s9, v74
	v_mul_u32_u24_e32 v55, 0x300, v75
	v_lshl_add_u32 v55, v76, 2, v55
	v_mul_u32_u24_e32 v67, 0x310, v75
	v_lshl_add_u32 v67, v76, 4, v67
	v_lshlrev_b32_e32 v74, 2, v55
	global_load_dwordx4 v[22:25], v74, s[72:73] nt
	ds_read_b128 v[100:103], v67
	v_lshlrev_b32_e32 v55, 1, v55
	v_or_b32_e32 v74, 3072, v0
	v_mul_u32_u24_e32 v75, 0xaab, v74
	v_lshrrev_b32_e32 v75, 17, v75
	v_mad_i32_i24 v76, v75, s9, v74
	v_mul_u32_u24_e32 v56, 0x300, v75
	v_lshl_add_u32 v56, v76, 2, v56
	v_mul_u32_u24_e32 v68, 0x310, v75
	v_lshl_add_u32 v68, v76, 4, v68
	v_lshlrev_b32_e32 v74, 2, v56
	global_load_dwordx4 v[26:29], v74, s[72:73] nt
	ds_read_b128 v[104:107], v68
	v_lshlrev_b32_e32 v56, 1, v56
	v_or_b32_e32 v74, 3584, v0
	v_mul_u32_u24_e32 v75, 0xaab, v74
	v_lshrrev_b32_e32 v75, 17, v75
	v_mad_i32_i24 v76, v75, s9, v74
	v_mul_u32_u24_e32 v57, 0x300, v75
	v_lshl_add_u32 v57, v76, 2, v57
	v_mul_u32_u24_e32 v69, 0x310, v75
	v_lshl_add_u32 v69, v76, 4, v69
	v_lshlrev_b32_e32 v74, 2, v57
	global_load_dwordx4 v[30:33], v74, s[72:73] nt
	ds_read_b128 v[108:111], v69
	v_lshlrev_b32_e32 v57, 1, v57
	v_or_b32_e32 v74, 4096, v0
	v_mul_u32_u24_e32 v75, 0xaab, v74
	v_lshrrev_b32_e32 v75, 17, v75
	v_mad_i32_i24 v76, v75, s9, v74
	v_mul_u32_u24_e32 v58, 0x300, v75
	v_lshl_add_u32 v58, v76, 2, v58
	v_mul_u32_u24_e32 v70, 0x310, v75
	v_lshl_add_u32 v70, v76, 4, v70
	v_lshlrev_b32_e32 v74, 2, v58
	global_load_dwordx4 v[34:37], v74, s[72:73] nt
	ds_read_b128 v[112:115], v70
	v_lshlrev_b32_e32 v58, 1, v58
	v_or_b32_e32 v74, 4608, v0
	v_mul_u32_u24_e32 v75, 0xaab, v74
	v_lshrrev_b32_e32 v75, 17, v75
	v_mad_i32_i24 v76, v75, s9, v74
	v_mul_u32_u24_e32 v59, 0x300, v75
	v_lshl_add_u32 v59, v76, 2, v59
	v_mul_u32_u24_e32 v71, 0x310, v75
	v_lshl_add_u32 v71, v76, 4, v71
	v_lshlrev_b32_e32 v74, 2, v59
	global_load_dwordx4 v[38:41], v74, s[72:73] nt
	ds_read_b128 v[116:119], v71
	v_lshlrev_b32_e32 v59, 1, v59
	v_or_b32_e32 v74, 5120, v0
	v_mul_u32_u24_e32 v75, 0xaab, v74
	v_lshrrev_b32_e32 v75, 17, v75
	v_mad_i32_i24 v76, v75, s9, v74
	v_mul_u32_u24_e32 v60, 0x300, v75
	v_lshl_add_u32 v60, v76, 2, v60
	v_mul_u32_u24_e32 v72, 0x310, v75
	v_lshl_add_u32 v72, v76, 4, v72
	v_lshlrev_b32_e32 v74, 2, v60
	global_load_dwordx4 v[42:45], v74, s[72:73] nt
	ds_read_b128 v[120:123], v72
	v_lshlrev_b32_e32 v60, 1, v60
	v_or_b32_e32 v74, 5632, v0
	v_mul_u32_u24_e32 v75, 0xaab, v74
	v_lshrrev_b32_e32 v75, 17, v75
	v_mad_i32_i24 v76, v75, s9, v74
	v_mul_u32_u24_e32 v61, 0x300, v75
	v_lshl_add_u32 v61, v76, 2, v61
	v_mul_u32_u24_e32 v73, 0x310, v75
	v_lshl_add_u32 v73, v76, 4, v73
	v_lshlrev_b32_e32 v74, 2, v61
	global_load_dwordx4 v[46:49], v74, s[72:73] nt
	ds_read_b128 v[124:127], v73
	v_lshlrev_b32_e32 v61, 1, v61
	s_waitcnt vmcnt(11) lgkmcnt(11)
	v_pk_add_f32 v[80:81], v[80:81], v[2:3]
	v_pk_add_f32 v[82:83], v[82:83], v[4:5]
	ds_write_b128 v62, v[80:83]
	v_cvt_pk_f16_f32 v2, v80, v81
	v_cvt_pk_f16_f32 v3, v82, v83
	global_store_dwordx2 v50, v[2:3], s[74:75]
	s_waitcnt vmcnt(11) lgkmcnt(11)
	v_pk_add_f32 v[84:85], v[84:85], v[6:7]
	v_pk_add_f32 v[86:87], v[86:87], v[8:9]
	ds_write_b128 v63, v[84:87]
	v_cvt_pk_f16_f32 v6, v84, v85
	v_cvt_pk_f16_f32 v7, v86, v87
	global_store_dwordx2 v51, v[6:7], s[74:75]
	s_waitcnt vmcnt(11) lgkmcnt(11)
	v_pk_add_f32 v[88:89], v[88:89], v[10:11]
	v_pk_add_f32 v[90:91], v[90:91], v[12:13]
	ds_write_b128 v64, v[88:91]
	v_cvt_pk_f16_f32 v10, v88, v89
	v_cvt_pk_f16_f32 v11, v90, v91
	global_store_dwordx2 v52, v[10:11], s[74:75]
	s_waitcnt vmcnt(11) lgkmcnt(11)
	v_pk_add_f32 v[92:93], v[92:93], v[14:15]
	v_pk_add_f32 v[94:95], v[94:95], v[16:17]
	ds_write_b128 v65, v[92:95]
	v_cvt_pk_f16_f32 v14, v92, v93
	v_cvt_pk_f16_f32 v15, v94, v95
	global_store_dwordx2 v53, v[14:15], s[74:75]
	s_waitcnt vmcnt(11) lgkmcnt(11)
	v_pk_add_f32 v[96:97], v[96:97], v[18:19]
	v_pk_add_f32 v[98:99], v[98:99], v[20:21]
	ds_write_b128 v66, v[96:99]
	v_cvt_pk_f16_f32 v18, v96, v97
	v_cvt_pk_f16_f32 v19, v98, v99
	global_store_dwordx2 v54, v[18:19], s[74:75]
	s_waitcnt vmcnt(11) lgkmcnt(11)
	v_pk_add_f32 v[100:101], v[100:101], v[22:23]
	v_pk_add_f32 v[102:103], v[102:103], v[24:25]
	ds_write_b128 v67, v[100:103]
	v_cvt_pk_f16_f32 v22, v100, v101
	v_cvt_pk_f16_f32 v23, v102, v103
	global_store_dwordx2 v55, v[22:23], s[74:75]
	s_waitcnt vmcnt(11) lgkmcnt(11)
	v_pk_add_f32 v[104:105], v[104:105], v[26:27]
	v_pk_add_f32 v[106:107], v[106:107], v[28:29]
	ds_write_b128 v68, v[104:107]
	v_cvt_pk_f16_f32 v26, v104, v105
	v_cvt_pk_f16_f32 v27, v106, v107
	global_store_dwordx2 v56, v[26:27], s[74:75]
	s_waitcnt vmcnt(11) lgkmcnt(11)
	v_pk_add_f32 v[108:109], v[108:109], v[30:31]
	v_pk_add_f32 v[110:111], v[110:111], v[32:33]
	ds_write_b128 v69, v[108:111]
	v_cvt_pk_f16_f32 v30, v108, v109
	v_cvt_pk_f16_f32 v31, v110, v111
	global_store_dwordx2 v57, v[30:31], s[74:75]
	s_waitcnt vmcnt(11) lgkmcnt(11)
	v_pk_add_f32 v[112:113], v[112:113], v[34:35]
	v_pk_add_f32 v[114:115], v[114:115], v[36:37]
	ds_write_b128 v70, v[112:115]
	v_cvt_pk_f16_f32 v34, v112, v113
	v_cvt_pk_f16_f32 v35, v114, v115
	global_store_dwordx2 v58, v[34:35], s[74:75]
	s_waitcnt vmcnt(11) lgkmcnt(11)
	v_pk_add_f32 v[116:117], v[116:117], v[38:39]
	v_pk_add_f32 v[118:119], v[118:119], v[40:41]
	ds_write_b128 v71, v[116:119]
	v_cvt_pk_f16_f32 v38, v116, v117
	v_cvt_pk_f16_f32 v39, v118, v119
	global_store_dwordx2 v59, v[38:39], s[74:75]
	s_waitcnt vmcnt(11) lgkmcnt(11)
	v_pk_add_f32 v[120:121], v[120:121], v[42:43]
	v_pk_add_f32 v[122:123], v[122:123], v[44:45]
	ds_write_b128 v72, v[120:123]
	v_cvt_pk_f16_f32 v42, v120, v121
	v_cvt_pk_f16_f32 v43, v122, v123
	global_store_dwordx2 v60, v[42:43], s[74:75]
	s_waitcnt vmcnt(11) lgkmcnt(11)
	v_pk_add_f32 v[124:125], v[124:125], v[46:47]
	v_pk_add_f32 v[126:127], v[126:127], v[48:49]
	ds_write_b128 v73, v[124:127]
	v_cvt_pk_f16_f32 v46, v124, v125
	v_cvt_pk_f16_f32 v47, v126, v127
	global_store_dwordx2 v61, v[46:47], s[74:75]
	v_lshrrev_b32_e32 v1, 2, v0
	v_and_b32_e32 v58, 3, v0
	v_mul_u32_u24_e32 v0, 0x310, v1
	v_mul_u32_u24_e32 v2, 0xc0, v58
	v_mov_b32_e32 v3, 0
	s_waitcnt lgkmcnt(0)
	s_barrier
	v_add3_u32 v0, 0, v0, v2
	ds_read_b128 v[4:7], v0
	ds_read_b128 v[8:11], v0 offset:16
	ds_read_b128 v[12:15], v0 offset:32
	ds_read_b128 v[16:19], v0 offset:48
	v_mov_b32_e32 v24, v3
	s_waitcnt lgkmcnt(3)
	v_mov_b32_e32 v20, v5
	v_mov_b32_e32 v21, v6
	v_mov_b32_e32 v22, v4
	v_mov_b32_e32 v23, v7
	v_pk_add_f32 v[20:21], v[20:21], v[22:23]
	s_waitcnt lgkmcnt(2)
	v_add_f32_e32 v2, v8, v9
	v_pk_add_f32 v[20:21], v[20:21], v[20:21] op_sel:[0,1] op_sel_hi:[1,0]
	v_add_f32_e32 v22, v10, v11
	s_waitcnt lgkmcnt(1)
	v_mov_b32_e32 v21, v12
	v_mov_b32_e32 v25, v13
	v_mov_b32_e32 v3, v14
	v_mov_b32_e32 v23, v15
	v_pk_add_f32 v[20:21], v[20:21], v[24:25]
	v_pk_add_f32 v[2:3], v[2:3], v[22:23]
	ds_read_b128 v[24:27], v0 offset:80
	v_pk_add_f32 v[2:3], v[20:21], v[2:3]
	ds_read_b128 v[20:23], v0 offset:64
	s_waitcnt lgkmcnt(2)
	v_mov_b32_e32 v28, v17
	v_mov_b32_e32 v29, v18
	v_mov_b32_e32 v30, v16
	v_mov_b32_e32 v31, v19
	v_pk_add_f32 v[28:29], v[28:29], v[30:31]
	v_pk_add_f32 v[2:3], v[2:3], v[2:3] op_sel:[0,1] op_sel_hi:[1,0]
	v_pk_add_f32 v[28:29], v[28:29], v[28:29] op_sel:[0,1] op_sel_hi:[1,0]
	s_waitcnt lgkmcnt(1)
	v_mov_b32_e32 v3, v24
	v_mov_b32_e32 v29, v25
	v_pk_add_f32 v[2:3], v[2:3], v[28:29]
	ds_read_b128 v[28:31], v0 offset:96
	s_waitcnt lgkmcnt(1)
	v_add_f32_e32 v32, v20, v21
	v_add_f32_e32 v34, v22, v23
	v_mov_b32_e32 v33, v26
	v_mov_b32_e32 v35, v27
	v_pk_add_f32 v[32:33], v[32:33], v[34:35]
	s_nop 0
	v_pk_add_f32 v[2:3], v[2:3], v[32:33]
	ds_read_b128 v[32:35], v0 offset:112
	s_waitcnt lgkmcnt(1)
	v_mov_b32_e32 v36, v29
	v_mov_b32_e32 v37, v30
	v_mov_b32_e32 v38, v28
	v_mov_b32_e32 v39, v31
	v_pk_add_f32 v[40:41], v[36:37], v[38:39]
	ds_read_b128 v[36:39], v0 offset:128
	v_pk_add_f32 v[2:3], v[2:3], v[2:3] op_sel:[0,1] op_sel_hi:[1,0]
	v_pk_add_f32 v[44:45], v[40:41], v[40:41] op_sel:[0,1] op_sel_hi:[1,0]
	ds_read_b128 v[40:43], v0 offset:144
	s_waitcnt lgkmcnt(2)
	v_add_f32_e32 v46, v32, v33
	v_add_f32_e32 v48, v34, v35
	s_waitcnt lgkmcnt(1)
	v_mov_b32_e32 v3, v36
	v_mov_b32_e32 v45, v37
	v_mov_b32_e32 v47, v38
	v_mov_b32_e32 v49, v39
	v_pk_add_f32 v[2:3], v[2:3], v[44:45]
	v_pk_add_f32 v[44:45], v[46:47], v[48:49]
	ds_read_b128 v[48:51], v0 offset:176
	v_pk_add_f32 v[2:3], v[2:3], v[44:45]
	ds_read_b128 v[44:47], v0 offset:160
	s_waitcnt lgkmcnt(2)
	v_mov_b32_e32 v52, v41
	v_mov_b32_e32 v53, v42
	v_mov_b32_e32 v54, v40
	v_mov_b32_e32 v55, v43
	v_pk_add_f32 v[52:53], v[52:53], v[54:55]
	v_pk_add_f32 v[2:3], v[2:3], v[2:3] op_sel:[0,1] op_sel_hi:[1,0]
	v_pk_add_f32 v[52:53], v[52:53], v[52:53] op_sel:[0,1] op_sel_hi:[1,0]
	s_waitcnt lgkmcnt(0)
	v_add_f32_e32 v54, v44, v45
	v_add_f32_e32 v56, v46, v47
	v_mov_b32_e32 v3, v48
	v_mov_b32_e32 v53, v49
	v_mov_b32_e32 v55, v50
	v_mov_b32_e32 v57, v51
	v_pk_add_f32 v[2:3], v[2:3], v[52:53]
	v_pk_add_f32 v[52:53], v[54:55], v[56:57]
	s_nop 0
	v_pk_add_f32 v[2:3], v[2:3], v[52:53]
	s_nop 0
	v_add_f32_e32 v0, v2, v3
	v_mbcnt_lo_u32_b32 v2, -1, 0
	v_mbcnt_hi_u32_b32 v2, -1, v2
	v_and_b32_e32 v52, 64, v2
	v_xor_b32_e32 v3, 1, v2
	v_add_u32_e32 v52, 64, v52
	v_cmp_lt_i32_e32 vcc, v3, v52
	s_nop 1
	v_cndmask_b32_e32 v3, v2, v3, vcc
	v_lshlrev_b32_e32 v3, 2, v3
	ds_bpermute_b32 v53, v3, v0
	s_waitcnt lgkmcnt(0)
	v_add_f32_e32 v0, v0, v53
	v_xor_b32_e32 v53, 2, v2
	v_cmp_lt_i32_e32 vcc, v53, v52
	s_nop 1
	v_cndmask_b32_e32 v2, v2, v53, vcc
	v_lshlrev_b32_e32 v52, 2, v2
	ds_bpermute_b32 v2, v52, v0
	v_cmp_eq_u32_e32 vcc, 0, v58
	s_waitcnt lgkmcnt(0)
	v_add_f32_e32 v0, v0, v2
	v_fmac_f32_e32 v5, 0xbbaaaaab, v0
	v_fmamk_f32 v2, v0, 0xbbaaaaab, v6
	v_fmamk_f32 v6, v0, 0xbbaaaaab, v7
	v_fmamk_f32 v4, v0, 0xbbaaaaab, v4
	v_mul_f32_e32 v5, v5, v5
	v_fmac_f32_e32 v5, v4, v4
	v_mul_f32_e32 v4, v6, v6
	v_fmac_f32_e32 v4, v2, v2
	v_add_f32_e32 v2, v5, v4
	v_fmamk_f32 v5, v0, 0xbbaaaaab, v11
	v_fmac_f32_e32 v9, 0xbbaaaaab, v0
	v_fmamk_f32 v4, v0, 0xbbaaaaab, v10
	v_fmamk_f32 v6, v0, 0xbbaaaaab, v8
	v_mul_f32_e32 v7, v9, v9
	v_mul_f32_e32 v5, v5, v5
	v_fmac_f32_e32 v7, v6, v6
	v_fmac_f32_e32 v5, v4, v4
	v_add_f32_e32 v4, v7, v5
	v_fmamk_f32 v5, v0, 0xbbaaaaab, v15
	v_fmac_f32_e32 v13, 0xbbaaaaab, v0
	v_add_f32_e32 v2, v2, v4
	v_fmamk_f32 v4, v0, 0xbbaaaaab, v14
	v_fmamk_f32 v6, v0, 0xbbaaaaab, v12
	v_mul_f32_e32 v7, v13, v13
	v_mul_f32_e32 v5, v5, v5
	v_fmac_f32_e32 v7, v6, v6
	v_fmac_f32_e32 v5, v4, v4
	v_add_f32_e32 v4, v7, v5
	v_fmamk_f32 v5, v0, 0xbbaaaaab, v19
	v_fmac_f32_e32 v17, 0xbbaaaaab, v0
	v_add_f32_e32 v2, v2, v4
	v_fmamk_f32 v4, v0, 0xbbaaaaab, v18
	v_fmamk_f32 v6, v0, 0xbbaaaaab, v16
	v_mul_f32_e32 v7, v17, v17
	v_mul_f32_e32 v5, v5, v5
	v_fmac_f32_e32 v7, v6, v6
	v_fmac_f32_e32 v5, v4, v4
	v_add_f32_e32 v4, v7, v5
	v_fmamk_f32 v5, v0, 0xbbaaaaab, v23
	v_fmac_f32_e32 v21, 0xbbaaaaab, v0
	v_add_f32_e32 v2, v2, v4
	v_fmamk_f32 v4, v0, 0xbbaaaaab, v22
	v_fmamk_f32 v6, v0, 0xbbaaaaab, v20
	v_mul_f32_e32 v7, v21, v21
	v_mul_f32_e32 v5, v5, v5
	v_fmac_f32_e32 v7, v6, v6
	v_fmac_f32_e32 v5, v4, v4
	v_add_f32_e32 v4, v7, v5
	v_fmamk_f32 v5, v0, 0xbbaaaaab, v27
	v_fmac_f32_e32 v25, 0xbbaaaaab, v0
	v_add_f32_e32 v2, v2, v4
	v_fmamk_f32 v4, v0, 0xbbaaaaab, v26
	v_fmamk_f32 v6, v0, 0xbbaaaaab, v24
	v_mul_f32_e32 v7, v25, v25
	v_mul_f32_e32 v5, v5, v5
	v_fmac_f32_e32 v7, v6, v6
	v_fmac_f32_e32 v5, v4, v4
	v_add_f32_e32 v4, v7, v5
	v_fmamk_f32 v5, v0, 0xbbaaaaab, v31
	v_fmac_f32_e32 v29, 0xbbaaaaab, v0
	v_add_f32_e32 v2, v2, v4
	v_fmamk_f32 v4, v0, 0xbbaaaaab, v30
	v_fmamk_f32 v6, v0, 0xbbaaaaab, v28
	v_mul_f32_e32 v7, v29, v29
	v_mul_f32_e32 v5, v5, v5
	v_fmac_f32_e32 v7, v6, v6
	v_fmac_f32_e32 v5, v4, v4
	v_add_f32_e32 v4, v7, v5
	v_fmamk_f32 v5, v0, 0xbbaaaaab, v35
	v_fmac_f32_e32 v33, 0xbbaaaaab, v0
	v_add_f32_e32 v2, v2, v4
	v_fmamk_f32 v4, v0, 0xbbaaaaab, v34
	v_fmamk_f32 v6, v0, 0xbbaaaaab, v32
	v_mul_f32_e32 v7, v33, v33
	v_mul_f32_e32 v5, v5, v5
	v_fmac_f32_e32 v7, v6, v6
	v_fmac_f32_e32 v5, v4, v4
	v_add_f32_e32 v4, v7, v5
	v_fmamk_f32 v5, v0, 0xbbaaaaab, v39
	v_fmac_f32_e32 v37, 0xbbaaaaab, v0
	v_add_f32_e32 v2, v2, v4
	v_fmamk_f32 v4, v0, 0xbbaaaaab, v38
	v_fmamk_f32 v6, v0, 0xbbaaaaab, v36
	v_mul_f32_e32 v7, v37, v37
	v_mul_f32_e32 v5, v5, v5
	v_fmac_f32_e32 v7, v6, v6
	v_fmac_f32_e32 v5, v4, v4
	v_add_f32_e32 v4, v7, v5
	v_fmamk_f32 v5, v0, 0xbbaaaaab, v43
	v_fmac_f32_e32 v41, 0xbbaaaaab, v0
	v_add_f32_e32 v2, v2, v4
	v_fmamk_f32 v4, v0, 0xbbaaaaab, v42
	v_fmamk_f32 v6, v0, 0xbbaaaaab, v40
	v_mul_f32_e32 v7, v41, v41
	v_mul_f32_e32 v5, v5, v5
	v_fmac_f32_e32 v7, v6, v6
	v_fmac_f32_e32 v5, v4, v4
	v_add_f32_e32 v4, v7, v5
	v_fmamk_f32 v5, v0, 0xbbaaaaab, v47
	v_fmac_f32_e32 v45, 0xbbaaaaab, v0
	v_add_f32_e32 v2, v2, v4
	v_fmamk_f32 v4, v0, 0xbbaaaaab, v46
	v_fmamk_f32 v6, v0, 0xbbaaaaab, v44
	v_mul_f32_e32 v7, v45, v45
	v_mul_f32_e32 v5, v5, v5
	v_fmac_f32_e32 v7, v6, v6
	v_fmac_f32_e32 v5, v4, v4
	v_add_f32_e32 v4, v7, v5
	v_fmamk_f32 v5, v0, 0xbbaaaaab, v51
	v_fmac_f32_e32 v49, 0xbbaaaaab, v0
	v_add_f32_e32 v2, v2, v4
	v_fmamk_f32 v4, v0, 0xbbaaaaab, v50
	v_fmamk_f32 v6, v0, 0xbbaaaaab, v48
	v_mul_f32_e32 v7, v49, v49
	v_mul_f32_e32 v5, v5, v5
	v_fmac_f32_e32 v7, v6, v6
	v_fmac_f32_e32 v5, v4, v4
	v_add_f32_e32 v4, v7, v5
	v_add_f32_e32 v2, v2, v4
	ds_bpermute_b32 v3, v3, v2
	s_waitcnt lgkmcnt(0)
	v_add_f32_e32 v2, v2, v3
	ds_bpermute_b32 v3, v52, v2
	s_and_saveexec_b64 s[0:1], vcc
	s_cbranch_execz .LBB4_8
	s_mul_hi_i32 s0, s8, 0x2aaaaaab
	s_lshr_b32 s1, s0, 31
	s_ashr_i32 s0, s0, 5
	v_mul_f32_e32 v4, 0x3baaaaab, v0
	v_add_u32_e32 v0, s3, v1
	s_add_i32 s0, s0, s1
	v_mov_b32_e32 v6, s6
	v_mov_b32_e32 v7, s7
	v_mad_i64_i32 v[0:1], s[0:1], v0, s0, 0
	s_ashr_i32 s3, s2, 31
	v_lshl_add_u64 v[0:1], v[0:1], 3, v[6:7]
	s_waitcnt lgkmcnt(0)
	v_add_f32_e32 v5, v2, v3
	v_lshl_add_u64 v[0:1], s[2:3], 3, v[0:1]
	global_store_dwordx2 v[0:1], v[4:5], off

	.amdhsa_kernel _Z6gemm_kILi1ELb1ELb0ELb1ELb1ELb0EEvPKtS1_ii7EpiArgs
		.amdhsa_group_segment_fixed_size 0
		.amdhsa_private_segment_fixed_size 0
		.amdhsa_kernarg_size 88
		.amdhsa_user_sgpr_count 2
		.amdhsa_user_sgpr_dispatch_ptr 0
		.amdhsa_user_sgpr_queue_ptr 0
		.amdhsa_user_sgpr_kernarg_segment_ptr 1
		.amdhsa_user_sgpr_dispatch_id 0
		.amdhsa_user_sgpr_kernarg_preload_length 0
		.amdhsa_user_sgpr_kernarg_preload_offset 0
		.amdhsa_user_sgpr_private_segment_size 0
		.amdhsa_uses_dynamic_stack 0
		.amdhsa_enable_private_segment 0
		.amdhsa_system_sgpr_workgroup_id_x 1
		.amdhsa_system_sgpr_workgroup_id_y 0
		.amdhsa_system_sgpr_workgroup_id_z 0
		.amdhsa_system_sgpr_workgroup_info 0
		.amdhsa_system_vgpr_workitem_id 0
		.amdhsa_next_free_vgpr 128
		.amdhsa_next_free_sgpr 76
		.amdhsa_accum_offset 128
		.amdhsa_reserve_vcc 1
		.amdhsa_float_round_mode_32 0
		.amdhsa_float_round_mode_16_64 0
		.amdhsa_float_denorm_mode_32 3
		.amdhsa_float_denorm_mode_16_64 3
		.amdhsa_dx10_clamp 1
		.amdhsa_ieee_mode 1
		.amdhsa_fp16_overflow 0
		.amdhsa_tg_split 0
		.amdhsa_exception_fp_ieee_invalid_op 0
		.amdhsa_exception_fp_denorm_src 0
		.amdhsa_exception_fp_ieee_div_zero 0
		.amdhsa_exception_fp_ieee_overflow 0
		.amdhsa_exception_fp_ieee_underflow 0
		.amdhsa_exception_fp_ieee_inexact 0
		.amdhsa_exception_int_div_zero 0
	.end_amdhsa_kernel

amdhsa.kernels:
  - .agpr_count:     0
    .args:
      - .offset:         0
        .size:           144
        .value_kind:     by_value
    .group_segment_fixed_size: 16640
    .kernarg_segment_align: 8
    .kernarg_segment_size: 144
    .language:       OpenCL C
    .language_version:
      - 2
      - 0
    .max_flat_workgroup_size: 256
    .name:           _Z8prep_ln18PrepArgs
    .private_segment_fixed_size: 0
    .sgpr_count:     18
    .sgpr_spill_count: 0
    .symbol:         _Z8prep_ln18PrepArgs.kd
    .uniform_work_group_size: 1
    .uses_dynamic_stack: false
    .vgpr_count:     61
    .vgpr_spill_count: 0
    .wavefront_size: 64
  - .agpr_count:     0
    .args:
      - .address_space:  global
        .offset:         0
        .size:           8
        .value_kind:     global_buffer
      - .address_space:  global
        .offset:         8
        .size:           8
        .value_kind:     global_buffer
      - .address_space:  global
        .offset:         16
        .size:           8
        .value_kind:     global_buffer
      - .address_space:  global
        .offset:         24
        .size:           8
        .value_kind:     global_buffer
      - .offset:         32
        .size:           144
        .value_kind:     by_value
    .group_segment_fixed_size: 0
    .kernarg_segment_align: 8
    .kernarg_segment_size: 176
    .language:       OpenCL C
    .language_version:
      - 2
      - 0
    .max_flat_workgroup_size: 256
    .name:           _Z10attn64_fwdPKtS0_S0_Pt8PrepArgs
    .private_segment_fixed_size: 0
    .sgpr_count:     42
    .sgpr_spill_count: 0
    .symbol:         _Z10attn64_fwdPKtS0_S0_Pt8PrepArgs.kd
    .uniform_work_group_size: 1
    .uses_dynamic_stack: false
    .vgpr_count:     221
    .vgpr_spill_count: 0
    .wavefront_size: 64
  - .agpr_count:     0
    .args:
      - .address_space:  global
        .offset:         0
        .size:           8
        .value_kind:     global_buffer
      - .address_space:  global
        .offset:         8
        .size:           8
        .value_kind:     global_buffer
      - .offset:         16
        .size:           4
        .value_kind:     by_value
      - .offset:         20
        .size:           4
        .value_kind:     by_value
      - .offset:         24
        .size:           64
        .value_kind:     by_value
    .group_segment_fixed_size: 0
    .kernarg_segment_align: 8
    .kernarg_segment_size: 88
    .language:       OpenCL C
    .language_version:
      - 2
      - 0
    .max_flat_workgroup_size: 256
    .name:           _Z8gemm2b_kILi2EEvPKtS1_ii7EpiArgs
    .private_segment_fixed_size: 0
    .sgpr_count:     98
    .sgpr_spill_count: 0
    .symbol:         _Z8gemm2b_kILi2EEvPKtS1_ii7EpiArgs.kd
    .uniform_work_group_size: 1
    .uses_dynamic_stack: false
    .vgpr_count:     212
    .vgpr_spill_count: 0
    .wavefront_size: 64
  - .agpr_count:     0
    .args:
      - .address_space:  global
        .offset:         0
        .size:           8
        .value_kind:     global_buffer
      - .address_space:  global
        .offset:         8
        .size:           8
        .value_kind:     global_buffer
      - .offset:         16
        .size:           4
        .value_kind:     by_value
      - .offset:         20
        .size:           4
        .value_kind:     by_value
      - .offset:         24
        .size:           64
        .value_kind:     by_value
    .group_segment_fixed_size: 0
    .kernarg_segment_align: 8
    .kernarg_segment_size: 88
    .language:       OpenCL C
    .language_version:
      - 2
      - 0
    .max_flat_workgroup_size: 256
    .name:           _Z8gemm2b_kILi0EEvPKtS1_ii7EpiArgs
    .private_segment_fixed_size: 0
    .sgpr_count:     85
    .sgpr_spill_count: 0
    .symbol:         _Z8gemm2b_kILi0EEvPKtS1_ii7EpiArgs.kd
    .uniform_work_group_size: 1
    .uses_dynamic_stack: false
    .vgpr_count:     186
    .vgpr_spill_count: 0
    .wavefront_size: 64
  - .agpr_count:     0
    .args:
      - .address_space:  global
        .offset:         0
        .size:           8
        .value_kind:     global_buffer
      - .address_space:  global
        .offset:         8
        .size:           8
        .value_kind:     global_buffer
      - .offset:         16
        .size:           4
        .value_kind:     by_value
      - .offset:         20
        .size:           4
        .value_kind:     by_value
      - .offset:         24
        .size:           64
        .value_kind:     by_value
    .group_segment_fixed_size: 0
    .kernarg_segment_align: 8
    .kernarg_segment_size: 88
    .language:       OpenCL C
    .language_version:
      - 2
      - 0
    .max_flat_workgroup_size: 512
    .name:           _Z6gemm_kILi1ELb1ELb0ELb1ELb1ELb0EEvPKtS1_ii7EpiArgs
    .private_segment_fixed_size: 0
    .sgpr_count:     82
    .sgpr_spill_count: 0
    .symbol:         _Z6gemm_kILi1ELb1ELb0ELb1ELb1ELb0EEvPKtS1_ii7EpiArgs.kd
    .uniform_work_group_size: 1
    .uses_dynamic_stack: false
    .vgpr_count:     128
    .vgpr_spill_count: 0
    .wavefront_size: 64
  - .agpr_count:     0
    .args:
      - .address_space:  global
        .offset:         0
        .size:           8
        .value_kind:     global_buffer
      - .address_space:  global
        .offset:         8
        .size:           8
        .value_kind:     global_buffer
      - .offset:         16
        .size:           4
        .value_kind:     by_value
      - .offset:         20
        .size:           4
        .value_kind:     by_value
      - .offset:         24
        .size:           64
        .value_kind:     by_value
    .group_segment_fixed_size: 0
    .kernarg_segment_align: 8
    .kernarg_segment_size: 88
    .language:       OpenCL C
    .language_version:
      - 2
      - 0
    .max_flat_workgroup_size: 512
    .name:           _Z6gemm_kILi1ELb1ELb1ELb0ELb0ELb1EEvPKtS1_ii7EpiArgs
    .private_segment_fixed_size: 0
    .sgpr_count:     84
    .sgpr_spill_count: 0
    .symbol:         _Z6gemm_kILi1ELb1ELb1ELb0ELb0ELb1EEvPKtS1_ii7EpiArgs.kd
    .uniform_work_group_size: 1
    .uses_dynamic_stack: false
    .vgpr_count:     224
    .vgpr_spill_count: 0
    .wavefront_size: 64
